# v37 + alignment barrier pair dropped (trailing half skips its last in-loop barrier; leading half starts its epilogue one interval early)
# baseline (speedup 1.0000x reference)
;     __device__ __forceinline__ void a_ready(const Unit&) const { if (++ncall == 3 && sig != nullptr && threadIdx.x == 0) __hip_atomic_fetch_add(sig, 1u, __ATOMIC_RELAXED, __HIP_MEMORY_SCOPE_AGENT); }
; #define PG8_STAGE(bufoff, gbase, voff) do { _Pragma("unroll") for (int _i = 0; _i < 2; ++_i) \
;         __builtin_amdgcn_global_load_lds((const unsigned*)((const char*)(gbase) + (voff)[_i]), (PG8_LAS unsigned*)(lds + (bufoff) + ldsw + _i * 8192), 16, 0, 0); } while (0)
; #define PG8_LDA(dst, b, h) do { _Pragma("unroll") for (int m = 0; m < 4; ++m) _Pragma("unroll") for (int k = 0; k < 2; ++k) dst[m][k] = *(const PG8_LAS bf16x8*)(lds + PG8_SA(b, h) + aoff + m * 2048 + k * 1024); } while (0)
; #define PG8_LDB(dst, b, h) do { _Pragma("unroll") for (int n = 0; n < 2; ++n) _Pragma("unroll") for (int k = 0; k < 2; ++k) dst[n][k] = *(const PG8_LAS bf16x8*)(lds + PG8_SB(b, h) + boff + n * 2048 + k * 1024); } while (0)
; #define PG8_WAIT_V(n) asm volatile("s_waitcnt vmcnt(" #n ")" ::: "memory")
; #define PG8_WAIT_L(n) asm volatile("s_waitcnt lgkmcnt(" #n ")" ::: "memory")
; #define PG8_BAR __builtin_amdgcn_s_barrier()
; #define PG8_SCHED __builtin_amdgcn_sched_barrier(0)
; template <class Epi, class Sched, bool ALIGN_EPI = false, bool SP2 = false>
; __device__ __forceinline__ void gemm_phase(PG8_LAS unsigned char* lds, const Gemm g, const Sched& S, const Epi& E) {
;     ...
;         for (int t = 0; t < nt; t += 2) {
;             const bool last = (t == nt - 2);
;             const char* a1 = cA + (size_t)(t + 1) * kstep;
;             const char* a2 = last ? nA : cA + (size_t)(t + 2) * kstep; const char* b2 = last ? nB : cB + (size_t)(t + 2) * kstep;
;             const char* a3 = a2 + kstep; const char* b3 = b2 + kstep;
;             if (last && has_next) S.a_ready(nxt);
;             if constexpr (SP2) {
;             PG8_LDB(B0, 0, 0); PG8_LDB(B1, 0, 1); PG8_SCHED; PG8_LDA(At, 0, 0); PG8_STAGE(PG8_SA(1, 1), a1 + hstep, voffA);
;     ...
;             if (PROBE_KIND == 18 && t == 0 && ui > 0 && g.probe) { const unsigned long long tq_ = __builtin_amdgcn_s_memrealtime(); PG8_WAIT_V(8); pg8_probe_acc += (unsigned)(__builtin_amdgcn_s_memrealtime() - tq_); }
;     ...
;             PG8_WAIT_V(8); PG8_WAIT_L(0); PG8_BAR; PG8_MMA(0, 0, At, B0); PG8_MMA(0, 1, At, B1); PG8_BAR; PG8_SCHED;
.LBB0_395:
	s_add_u32 s0, s8, 0xfffc0080
	s_addc_u32 s1, s9, -1
	s_add_i32 s61, 0, 0x10000
	s_cmp_eq_u32 s39, 12
	s_cselect_b32 s11, s12, s1
	s_cselect_b32 s10, s13, s0
	v_add_u32_e32 v2, s61, v203
	s_cselect_b32 s1, s14, s38
	s_cselect_b32 s0, s15, s36
	s_add_i32 s63, 0, 0x14000
	ds_read_b128 v[132:135], v2
	ds_read_b128 v[136:139], v2 offset:1024
	ds_read_b128 v[140:143], v2 offset:2048
	ds_read_b128 v[144:147], v2 offset:3072
	v_add_u32_e32 v2, s63, v203
	ds_read_b128 v[148:151], v2
	ds_read_b128 v[152:155], v2 offset:1024
	ds_read_b128 v[156:159], v2 offset:2048
	ds_read_b128 v[160:163], v2 offset:3072
	v_lshl_add_u64 v[228:229], s[8:9], 0, v[178:179]
	s_add_i32 m0, s19, 0xc000
	ds_read_b128 v[182:185], v206
	ds_read_b128 v[186:189], v206 offset:1024
	ds_read_b128 v[190:193], v206 offset:2048
	ds_read_b128 v[194:197], v206 offset:3072
	ds_read_b128 v[198:201], v206 offset:4096
	ds_read_b128 v[208:211], v206 offset:5120
	ds_read_b128 v[212:215], v206 offset:6144
	ds_read_b128 v[216:219], v206 offset:7168
	global_load_lds_dwordx4 v[228:229], off
	v_lshl_add_u64 v[228:229], s[8:9], 0, v[180:181]
	s_add_i32 m0, s19, 0xe000
	s_nop 0
	global_load_lds_dwordx4 v[228:229], off
	s_waitcnt vmcnt(8)
	s_waitcnt lgkmcnt(0)
	s_barrier
	s_setprio 1
	s_waitcnt lgkmcnt(0)
	v_mfma_f32_16x16x32_bf16 v[128:131], v[132:135], v[182:185], v[128:131]
	v_mfma_f32_16x16x32_bf16 v[124:127], v[140:143], v[182:185], v[124:127]
	v_mfma_f32_16x16x32_bf16 v[112:115], v[132:135], v[190:193], v[112:115]
	v_mfma_f32_16x16x32_bf16 v[108:111], v[140:143], v[190:193], v[108:111]
	v_mfma_f32_16x16x32_bf16 v[96:99], v[132:135], v[198:201], v[96:99]
	v_mfma_f32_16x16x32_bf16 v[92:95], v[140:143], v[198:201], v[92:95]
	v_mfma_f32_16x16x32_bf16 v[80:83], v[132:135], v[212:215], v[80:83]
	v_mfma_f32_16x16x32_bf16 v[76:79], v[140:143], v[212:215], v[76:79]
	v_mfma_f32_16x16x32_bf16 v[128:131], v[136:139], v[186:189], v[128:131]
	v_mfma_f32_16x16x32_bf16 v[124:127], v[144:147], v[186:189], v[124:127]
	v_mfma_f32_16x16x32_bf16 v[112:115], v[136:139], v[194:197], v[112:115]
	v_mfma_f32_16x16x32_bf16 v[108:111], v[144:147], v[194:197], v[108:111]
	v_mfma_f32_16x16x32_bf16 v[96:99], v[136:139], v[208:211], v[96:99]
	v_mfma_f32_16x16x32_bf16 v[92:95], v[144:147], v[208:211], v[92:95]
	v_mfma_f32_16x16x32_bf16 v[80:83], v[136:139], v[216:219], v[80:83]
	v_mfma_f32_16x16x32_bf16 v[76:79], v[144:147], v[216:219], v[76:79]
	s_setprio 0
	s_setprio 1
	v_mfma_f32_16x16x32_bf16 v[120:123], v[148:151], v[182:185], v[120:123]
	v_mfma_f32_16x16x32_bf16 v[116:119], v[156:159], v[182:185], v[116:119]
	v_mfma_f32_16x16x32_bf16 v[104:107], v[148:151], v[190:193], v[104:107]
	v_mfma_f32_16x16x32_bf16 v[100:103], v[156:159], v[190:193], v[100:103]
	v_mfma_f32_16x16x32_bf16 v[88:91], v[148:151], v[198:201], v[88:91]
	v_mfma_f32_16x16x32_bf16 v[84:87], v[156:159], v[198:201], v[84:87]
	v_mfma_f32_16x16x32_bf16 v[72:75], v[148:151], v[212:215], v[72:75]
	v_mfma_f32_16x16x32_bf16 v[68:71], v[156:159], v[212:215], v[68:71]
	v_mfma_f32_16x16x32_bf16 v[120:123], v[152:155], v[186:189], v[120:123]
	v_mfma_f32_16x16x32_bf16 v[116:119], v[160:163], v[186:189], v[116:119]
	v_mfma_f32_16x16x32_bf16 v[104:107], v[152:155], v[194:197], v[104:107]
	v_mfma_f32_16x16x32_bf16 v[100:103], v[160:163], v[194:197], v[100:103]
	v_mfma_f32_16x16x32_bf16 v[88:91], v[152:155], v[208:211], v[88:91]
	v_mfma_f32_16x16x32_bf16 v[84:87], v[160:163], v[208:211], v[84:87]
	v_mfma_f32_16x16x32_bf16 v[72:75], v[152:155], v[216:219], v[72:75]
	v_mfma_f32_16x16x32_bf16 v[68:71], v[160:163], v[216:219], v[68:71]
	s_setprio 0
	s_barrier
	s_add_i32 s61, s61, s27
	v_lshl_add_u64 v[228:229], s[0:1], 0, v[166:167]
	s_mov_b32 m0, s61
	ds_read_b128 v[182:185], v206 offset:16384
	ds_read_b128 v[186:189], v206 offset:17408
	ds_read_b128 v[190:193], v206 offset:18432
	ds_read_b128 v[194:197], v206 offset:19456
	ds_read_b128 v[198:201], v206 offset:20480
	ds_read_b128 v[208:211], v206 offset:21504
	ds_read_b128 v[212:215], v206 offset:22528
	ds_read_b128 v[216:219], v206 offset:23552
	global_load_lds_dwordx4 v[228:229], off
	s_add_i32 m0, s61, 0x2000
	s_add_u32 s78, s0, 0x40000
	v_lshl_add_u64 v[230:231], s[0:1], 0, v[170:171]
	s_addc_u32 s79, s1, 0
	s_add_i32 s61, s63, s27
	global_load_lds_dwordx4 v[230:231], off
	v_lshl_add_u64 v[232:233], s[78:79], 0, v[166:167]
	s_mov_b32 m0, s61
	v_lshl_add_u64 v[234:235], s[10:11], 0, v[168:169]
	global_load_lds_dwordx4 v[232:233], off
	v_lshl_add_u64 v[232:233], s[78:79], 0, v[170:171]
	s_add_i32 m0, s61, 0x2000
	s_nop 0
	global_load_lds_dwordx4 v[232:233], off
	v_lshl_add_u64 v[232:233], s[10:11], 0, v[164:165]
	s_mov_b32 m0, s19
	s_nop 0
	global_load_lds_dwordx4 v[232:233], off
	s_mov_b32 m0, s30
	s_nop 0
	global_load_lds_dwordx4 v[234:235], off
	s_waitcnt vmcnt(8)
	s_waitcnt lgkmcnt(0)
	s_barrier
; #define PG8_STAGE(bufoff, gbase, voff) do { _Pragma("unroll") for (int _i = 0; _i < 2; ++_i) \
;         __builtin_amdgcn_global_load_lds((const unsigned*)((const char*)(gbase) + (voff)[_i]), (PG8_LAS unsigned*)(lds + (bufoff) + ldsw + _i * 8192), 16, 0, 0); } while (0)
; #define PG8_LDA(dst, b, h) do { _Pragma("unroll") for (int m = 0; m < 4; ++m) _Pragma("unroll") for (int k = 0; k < 2; ++k) dst[m][k] = *(const PG8_LAS bf16x8*)(lds + PG8_SA(b, h) + aoff + m * 2048 + k * 1024); } while (0)
; #define PG8_LDB(dst, b, h) do { _Pragma("unroll") for (int n = 0; n < 2; ++n) _Pragma("unroll") for (int k = 0; k < 2; ++k) dst[n][k] = *(const PG8_LAS bf16x8*)(lds + PG8_SB(b, h) + boff + n * 2048 + k * 1024); } while (0)
; #define PG8_MMA(ai, bj, At, Bt) do { __builtin_amdgcn_s_setprio(1); _Pragma("unroll") for (int m = 0; m < 4; ++m) _Pragma("unroll") for (int n = 0; n < 2; ++n) _Pragma("unroll") for (int k = 0; k < 2; ++k) \
;         acc[ai][bj][m][n] = __builtin_amdgcn_mfma_f32_16x16x32_bf16(Bt[n][k], At[m][k], acc[ai][bj][m][n], 0, 0, 0); __builtin_amdgcn_s_setprio(0); } while (0)
; #define PG8_WAIT_V(n) asm volatile("s_waitcnt vmcnt(" #n ")" ::: "memory")
; #define PG8_WAIT_L(n) asm volatile("s_waitcnt lgkmcnt(" #n ")" ::: "memory")
; #define PG8_BAR __builtin_amdgcn_s_barrier()
; #define PG8_SCHED __builtin_amdgcn_sched_barrier(0)
; template <class Epi, class Sched, bool ALIGN_EPI = false, bool SP2 = false>
; __device__ __forceinline__ void gemm_phase(PG8_LAS unsigned char* lds, const Gemm g, const Sched& S, const Epi& E) {
;     ...
;             PG8_WAIT_V(8); PG8_WAIT_L(0); PG8_BAR; if (cur.half == 0) { PG8_MMA(1, 0, At, B0); PG8_MMA(1, 1, At, B1); } PG8_BAR; PG8_SCHED;
;             PG8_LDB(B0, 1, 0); PG8_LDB(B1, 1, 1); PG8_SCHED; PG8_LDA(At, 1, 0); PG8_STAGE(PG8_SA(0, 1), a2 + hstep, voffA);
;             PG8_WAIT_V(8); PG8_WAIT_L(0); PG8_BAR; PG8_MMA(0, 0, At, B0); PG8_MMA(0, 1, At, B1); PG8_BAR; PG8_SCHED;
	s_setprio 1
	s_waitcnt lgkmcnt(0)
	v_mfma_f32_16x16x32_bf16 v[64:67], v[132:135], v[182:185], v[64:67]
	v_mfma_f32_16x16x32_bf16 v[60:63], v[140:143], v[182:185], v[60:63]
	v_mfma_f32_16x16x32_bf16 v[48:51], v[132:135], v[190:193], v[48:51]
	v_mfma_f32_16x16x32_bf16 v[44:47], v[140:143], v[190:193], v[44:47]
	v_mfma_f32_16x16x32_bf16 v[32:35], v[132:135], v[198:201], v[32:35]
	v_mfma_f32_16x16x32_bf16 v[28:31], v[140:143], v[198:201], v[28:31]
	v_mfma_f32_16x16x32_bf16 v[16:19], v[132:135], v[212:215], v[16:19]
	v_mfma_f32_16x16x32_bf16 v[12:15], v[140:143], v[212:215], v[12:15]
	v_mfma_f32_16x16x32_bf16 v[64:67], v[136:139], v[186:189], v[64:67]
	v_mfma_f32_16x16x32_bf16 v[60:63], v[144:147], v[186:189], v[60:63]
	v_mfma_f32_16x16x32_bf16 v[48:51], v[136:139], v[194:197], v[48:51]
	v_mfma_f32_16x16x32_bf16 v[44:47], v[144:147], v[194:197], v[44:47]
	v_mfma_f32_16x16x32_bf16 v[32:35], v[136:139], v[208:211], v[32:35]
	v_mfma_f32_16x16x32_bf16 v[28:31], v[144:147], v[208:211], v[28:31]
	v_mfma_f32_16x16x32_bf16 v[16:19], v[136:139], v[216:219], v[16:19]
	v_mfma_f32_16x16x32_bf16 v[12:15], v[144:147], v[216:219], v[12:15]
	s_setprio 0
	s_setprio 1
	v_mfma_f32_16x16x32_bf16 v[56:59], v[148:151], v[182:185], v[56:59]
	v_mfma_f32_16x16x32_bf16 v[52:55], v[156:159], v[182:185], v[52:55]
	v_mfma_f32_16x16x32_bf16 v[40:43], v[148:151], v[190:193], v[40:43]
	v_mfma_f32_16x16x32_bf16 v[36:39], v[156:159], v[190:193], v[36:39]
	v_mfma_f32_16x16x32_bf16 v[24:27], v[148:151], v[198:201], v[24:27]
	v_mfma_f32_16x16x32_bf16 v[20:23], v[156:159], v[198:201], v[20:23]
	v_mfma_f32_16x16x32_bf16 v[8:11], v[148:151], v[212:215], v[8:11]
	v_mfma_f32_16x16x32_bf16 v[4:7], v[156:159], v[212:215], v[4:7]
	v_mfma_f32_16x16x32_bf16 v[56:59], v[152:155], v[186:189], v[56:59]
	v_mfma_f32_16x16x32_bf16 v[52:55], v[160:163], v[186:189], v[52:55]
	v_mfma_f32_16x16x32_bf16 v[40:43], v[152:155], v[194:197], v[40:43]
	v_mfma_f32_16x16x32_bf16 v[36:39], v[160:163], v[194:197], v[36:39]
	v_mfma_f32_16x16x32_bf16 v[24:27], v[152:155], v[208:211], v[24:27]
	v_mfma_f32_16x16x32_bf16 v[20:23], v[160:163], v[208:211], v[20:23]
	v_mfma_f32_16x16x32_bf16 v[8:11], v[152:155], v[216:219], v[8:11]
	v_mfma_f32_16x16x32_bf16 v[4:7], v[160:163], v[216:219], v[4:7]
	s_setprio 0
	s_barrier
	s_add_i32 s61, 0, 0x18000
	v_add_u32_e32 v2, s61, v203
	s_add_i32 s63, 0, 0x1c000
	ds_read_b128 v[132:135], v2
	ds_read_b128 v[136:139], v2 offset:1024
	ds_read_b128 v[140:143], v2 offset:2048
	ds_read_b128 v[144:147], v2 offset:3072
	v_add_u32_e32 v2, s63, v203
	ds_read_b128 v[148:151], v2
	ds_read_b128 v[152:155], v2 offset:1024
	ds_read_b128 v[156:159], v2 offset:2048
	ds_read_b128 v[160:163], v2 offset:3072
	s_add_u32 s10, s10, 0x40000
	s_addc_u32 s11, s11, 0
	s_mov_b32 m0, s31
	v_lshl_add_u64 v[236:237], s[10:11], 0, v[164:165]
	ds_read_b128 v[182:185], v206 offset:32768
	ds_read_b128 v[186:189], v206 offset:33792
	ds_read_b128 v[190:193], v206 offset:34816
	ds_read_b128 v[194:197], v206 offset:35840
	ds_read_b128 v[198:201], v206 offset:36864
	ds_read_b128 v[208:211], v206 offset:37888
	ds_read_b128 v[212:215], v206 offset:38912
	ds_read_b128 v[216:219], v206 offset:39936
	global_load_lds_dwordx4 v[236:237], off
	v_lshl_add_u64 v[236:237], s[10:11], 0, v[168:169]
	s_mov_b32 m0, s34
	s_nop 0
	global_load_lds_dwordx4 v[236:237], off
	s_waitcnt vmcnt(8)
	s_waitcnt lgkmcnt(0)
	s_barrier
	s_setprio 1
	s_waitcnt lgkmcnt(0)
	v_mfma_f32_16x16x32_bf16 v[128:131], v[132:135], v[182:185], v[128:131]
	v_mfma_f32_16x16x32_bf16 v[124:127], v[140:143], v[182:185], v[124:127]
	v_mfma_f32_16x16x32_bf16 v[112:115], v[132:135], v[190:193], v[112:115]
	v_mfma_f32_16x16x32_bf16 v[108:111], v[140:143], v[190:193], v[108:111]
	v_mfma_f32_16x16x32_bf16 v[96:99], v[132:135], v[198:201], v[96:99]
	v_mfma_f32_16x16x32_bf16 v[92:95], v[140:143], v[198:201], v[92:95]
	v_mfma_f32_16x16x32_bf16 v[80:83], v[132:135], v[212:215], v[80:83]
	v_mfma_f32_16x16x32_bf16 v[76:79], v[140:143], v[212:215], v[76:79]
	v_mfma_f32_16x16x32_bf16 v[128:131], v[136:139], v[186:189], v[128:131]
	v_mfma_f32_16x16x32_bf16 v[124:127], v[144:147], v[186:189], v[124:127]
	v_mfma_f32_16x16x32_bf16 v[112:115], v[136:139], v[194:197], v[112:115]
	v_mfma_f32_16x16x32_bf16 v[108:111], v[144:147], v[194:197], v[108:111]
	v_mfma_f32_16x16x32_bf16 v[96:99], v[136:139], v[208:211], v[96:99]
	v_mfma_f32_16x16x32_bf16 v[92:95], v[144:147], v[208:211], v[92:95]
	v_mfma_f32_16x16x32_bf16 v[80:83], v[136:139], v[216:219], v[80:83]
	v_mfma_f32_16x16x32_bf16 v[76:79], v[144:147], v[216:219], v[76:79]
	s_setprio 0
	s_setprio 1
	v_mfma_f32_16x16x32_bf16 v[120:123], v[148:151], v[182:185], v[120:123]
	v_mfma_f32_16x16x32_bf16 v[116:119], v[156:159], v[182:185], v[116:119]
	v_mfma_f32_16x16x32_bf16 v[104:107], v[148:151], v[190:193], v[104:107]
	v_mfma_f32_16x16x32_bf16 v[100:103], v[156:159], v[190:193], v[100:103]
	v_mfma_f32_16x16x32_bf16 v[88:91], v[148:151], v[198:201], v[88:91]
	v_mfma_f32_16x16x32_bf16 v[84:87], v[156:159], v[198:201], v[84:87]
	v_mfma_f32_16x16x32_bf16 v[72:75], v[148:151], v[212:215], v[72:75]
	v_mfma_f32_16x16x32_bf16 v[68:71], v[156:159], v[212:215], v[68:71]
	v_mfma_f32_16x16x32_bf16 v[120:123], v[152:155], v[186:189], v[120:123]
	v_mfma_f32_16x16x32_bf16 v[116:119], v[160:163], v[186:189], v[116:119]
	v_mfma_f32_16x16x32_bf16 v[104:107], v[152:155], v[194:197], v[104:107]
	v_mfma_f32_16x16x32_bf16 v[100:103], v[160:163], v[194:197], v[100:103]
	v_mfma_f32_16x16x32_bf16 v[88:91], v[152:155], v[208:211], v[88:91]
	v_mfma_f32_16x16x32_bf16 v[84:87], v[160:163], v[208:211], v[84:87]
	v_mfma_f32_16x16x32_bf16 v[72:75], v[152:155], v[216:219], v[72:75]
	v_mfma_f32_16x16x32_bf16 v[68:71], v[160:163], v[216:219], v[68:71]
	s_setprio 0
	s_barrier
; #define PG8_STAGE(bufoff, gbase, voff) do { _Pragma("unroll") for (int _i = 0; _i < 2; ++_i) \
;         __builtin_amdgcn_global_load_lds((const unsigned*)((const char*)(gbase) + (voff)[_i]), (PG8_LAS unsigned*)(lds + (bufoff) + ldsw + _i * 8192), 16, 0, 0); } while (0)
; #define PG8_LDA(dst, b, h) do { _Pragma("unroll") for (int m = 0; m < 4; ++m) _Pragma("unroll") for (int k = 0; k < 2; ++k) dst[m][k] = *(const PG8_LAS bf16x8*)(lds + PG8_SA(b, h) + aoff + m * 2048 + k * 1024); } while (0)
; #define PG8_MMA(ai, bj, At, Bt) do { __builtin_amdgcn_s_setprio(1); _Pragma("unroll") for (int m = 0; m < 4; ++m) _Pragma("unroll") for (int n = 0; n < 2; ++n) _Pragma("unroll") for (int k = 0; k < 2; ++k) \
;         acc[ai][bj][m][n] = __builtin_amdgcn_mfma_f32_16x16x32_bf16(Bt[n][k], At[m][k], acc[ai][bj][m][n], 0, 0, 0); __builtin_amdgcn_s_setprio(0); } while (0)
; #define PG8_WAIT_V(n) asm volatile("s_waitcnt vmcnt(" #n ")" ::: "memory")
; #define PG8_WAIT_L(n) asm volatile("s_waitcnt lgkmcnt(" #n ")" ::: "memory")
; #define PG8_BAR __builtin_amdgcn_s_barrier()
; #define PG8_SCHED __builtin_amdgcn_sched_barrier(0)
; template <class Epi, class Sched, bool ALIGN_EPI = false, bool SP2 = false>
; __device__ __forceinline__ void gemm_phase(PG8_LAS unsigned char* lds, const Gemm g, const Sched& S, const Epi& E) {
;     ...
;             PG8_LDA(At, 1, 1); PG8_STAGE(PG8_SB(1, 0), b3, voffB); PG8_STAGE(PG8_SB(1, 1), b3 + hstep, voffB); PG8_STAGE(PG8_SA(1, 0), a3, voffA);
;             PG8_WAIT_V(8); PG8_WAIT_L(0); PG8_BAR; if (cur.half == 0) { PG8_MMA(1, 0, At, B0); PG8_MMA(1, 1, At, B1); } PG8_BAR; PG8_SCHED;
;     ...
;         }
;         if constexpr (ALIGN_EPI) { if (wr == 0) PG8_BAR; }
	s_add_i32 s10, s61, s27
	v_lshl_add_u64 v[228:229], v[228:229], 0, s[42:43]
	s_mov_b32 m0, s10
	ds_read_b128 v[182:185], v206 offset:49152
	ds_read_b128 v[186:189], v206 offset:50176
	ds_read_b128 v[190:193], v206 offset:51200
	ds_read_b128 v[194:197], v206 offset:52224
	ds_read_b128 v[198:201], v206 offset:53248
	ds_read_b128 v[208:211], v206 offset:54272
	ds_read_b128 v[212:215], v206 offset:55296
	ds_read_b128 v[216:219], v206 offset:56320
	global_load_lds_dwordx4 v[228:229], off
	s_add_i32 m0, s10, 0x2000
	s_add_u32 s0, s0, 0x40080
	v_lshl_add_u64 v[228:229], v[230:231], 0, s[42:43]
	s_addc_u32 s1, s1, 0
	s_add_i32 s10, s63, s27
	global_load_lds_dwordx4 v[228:229], off
	v_lshl_add_u64 v[228:229], s[0:1], 0, v[166:167]
	s_mov_b32 m0, s10
	s_nop 0
	global_load_lds_dwordx4 v[228:229], off
	v_lshl_add_u64 v[228:229], s[0:1], 0, v[170:171]
	s_add_i32 m0, s10, 0x2000
	s_nop 0
	global_load_lds_dwordx4 v[228:229], off
	v_lshl_add_u64 v[228:229], v[232:233], 0, s[42:43]
	s_mov_b32 m0, s41
	s_nop 0
	global_load_lds_dwordx4 v[228:229], off
	v_lshl_add_u64 v[228:229], v[234:235], 0, s[42:43]
	s_mov_b32 m0, s71
	s_nop 0
	global_load_lds_dwordx4 v[228:229], off
	s_waitcnt vmcnt(8)
	s_waitcnt lgkmcnt(0)
	s_barrier
	s_setprio 1
	s_waitcnt lgkmcnt(0)
	v_mfma_f32_16x16x32_bf16 v[64:67], v[132:135], v[182:185], v[64:67]
	v_mfma_f32_16x16x32_bf16 v[60:63], v[140:143], v[182:185], v[60:63]
	v_mfma_f32_16x16x32_bf16 v[48:51], v[132:135], v[190:193], v[48:51]
	v_mfma_f32_16x16x32_bf16 v[44:47], v[140:143], v[190:193], v[44:47]
	v_mfma_f32_16x16x32_bf16 v[32:35], v[132:135], v[198:201], v[32:35]
	v_mfma_f32_16x16x32_bf16 v[28:31], v[140:143], v[198:201], v[28:31]
	v_mfma_f32_16x16x32_bf16 v[16:19], v[132:135], v[212:215], v[16:19]
	v_mfma_f32_16x16x32_bf16 v[12:15], v[140:143], v[212:215], v[12:15]
	v_mfma_f32_16x16x32_bf16 v[64:67], v[136:139], v[186:189], v[64:67]
	v_mfma_f32_16x16x32_bf16 v[60:63], v[144:147], v[186:189], v[60:63]
	v_mfma_f32_16x16x32_bf16 v[48:51], v[136:139], v[194:197], v[48:51]
	v_mfma_f32_16x16x32_bf16 v[44:47], v[144:147], v[194:197], v[44:47]
	v_mfma_f32_16x16x32_bf16 v[32:35], v[136:139], v[208:211], v[32:35]
	v_mfma_f32_16x16x32_bf16 v[28:31], v[144:147], v[208:211], v[28:31]
	v_mfma_f32_16x16x32_bf16 v[16:19], v[136:139], v[216:219], v[16:19]
	v_mfma_f32_16x16x32_bf16 v[12:15], v[144:147], v[216:219], v[12:15]
	s_setprio 0
	s_setprio 1
	v_mfma_f32_16x16x32_bf16 v[56:59], v[148:151], v[182:185], v[56:59]
	v_mfma_f32_16x16x32_bf16 v[52:55], v[156:159], v[182:185], v[52:55]
	v_mfma_f32_16x16x32_bf16 v[40:43], v[148:151], v[190:193], v[40:43]
	v_mfma_f32_16x16x32_bf16 v[36:39], v[156:159], v[190:193], v[36:39]
	v_mfma_f32_16x16x32_bf16 v[24:27], v[148:151], v[198:201], v[24:27]
	v_mfma_f32_16x16x32_bf16 v[20:23], v[156:159], v[198:201], v[20:23]
	v_mfma_f32_16x16x32_bf16 v[8:11], v[148:151], v[212:215], v[8:11]
	v_mfma_f32_16x16x32_bf16 v[4:7], v[156:159], v[212:215], v[4:7]
	v_mfma_f32_16x16x32_bf16 v[56:59], v[152:155], v[186:189], v[56:59]
	v_mfma_f32_16x16x32_bf16 v[52:55], v[160:163], v[186:189], v[52:55]
	v_mfma_f32_16x16x32_bf16 v[40:43], v[152:155], v[194:197], v[40:43]
	v_mfma_f32_16x16x32_bf16 v[36:39], v[160:163], v[194:197], v[36:39]
	v_mfma_f32_16x16x32_bf16 v[24:27], v[152:155], v[208:211], v[24:27]
	v_mfma_f32_16x16x32_bf16 v[20:23], v[160:163], v[208:211], v[20:23]
	v_mfma_f32_16x16x32_bf16 v[8:11], v[152:155], v[216:219], v[8:11]
	v_mfma_f32_16x16x32_bf16 v[4:7], v[160:163], v[216:219], v[4:7]
	s_setprio 0
	s_add_i32 s39, s39, 2
	s_add_u32 s8, s8, 0x100
	s_addc_u32 s9, s9, 0
	s_add_u32 s36, s36, 0x100
	s_addc_u32 s38, s38, 0
	s_cmp_gt_u32 s39, 13
	s_cbranch_scc1 .Lee_ip
	s_barrier
	s_branch .LBB0_395
.Lee_ip:
	s_and_b64 vcc, exec, s[58:59]
	s_cbranch_vccz .LBB0_398
	s_barrier

; #define PG8_MMA(ai, bj, At, Bt) do { __builtin_amdgcn_s_setprio(1); _Pragma("unroll") for (int m = 0; m < 4; ++m) _Pragma("unroll") for (int n = 0; n < 2; ++n) _Pragma("unroll") for (int k = 0; k < 2; ++k) \
;         acc[ai][bj][m][n] = __builtin_amdgcn_mfma_f32_16x16x32_bf16(Bt[n][k], At[m][k], acc[ai][bj][m][n], 0, 0, 0); __builtin_amdgcn_s_setprio(0); } while (0)
; #define PG8_WAIT_V(n) asm volatile("s_waitcnt vmcnt(" #n ")" ::: "memory")
; #define PG8_WAIT_L(n) asm volatile("s_waitcnt lgkmcnt(" #n ")" ::: "memory")
; #define PG8_BAR __builtin_amdgcn_s_barrier()
; #define PG8_SCHED __builtin_amdgcn_sched_barrier(0)
; template <class Epi, class Sched, bool ALIGN_EPI = false, bool SP2 = false>
; __device__ __forceinline__ void gemm_phase(PG8_LAS unsigned char* lds, const Gemm g, const Sched& S, const Epi& E) {
;     ...
;             PG8_WAIT_V(8); PG8_WAIT_L(0); PG8_BAR; if (cur.half == 0) { PG8_MMA(1, 0, At, B0); PG8_MMA(1, 1, At, B1); } PG8_BAR; PG8_SCHED;
;     ...
;         }
;         if constexpr (ALIGN_EPI) { if (wr == 0) PG8_BAR; }
.Lmg_nopf:
	s_waitcnt lgkmcnt(0)
	s_barrier
	s_setprio 1
	s_waitcnt lgkmcnt(0)
	v_mfma_f32_16x16x32_bf16 v[96:99], v[68:71], v[174:177], v[96:99]
	v_mfma_f32_16x16x32_bf16 v[92:95], v[76:79], v[174:177], v[92:95]
	v_mfma_f32_16x16x32_bf16 v[64:67], v[68:71], v[182:185], v[64:67]
	v_mfma_f32_16x16x32_bf16 v[60:63], v[76:79], v[182:185], v[60:63]
	v_mfma_f32_16x16x32_bf16 v[32:35], v[68:71], v[190:193], v[32:35]
	v_mfma_f32_16x16x32_bf16 v[28:31], v[76:79], v[190:193], v[28:31]
	v_mfma_f32_16x16x32_bf16 v[16:19], v[68:71], v[204:207], v[16:19]
	v_mfma_f32_16x16x32_bf16 v[12:15], v[76:79], v[204:207], v[12:15]
	v_mfma_f32_16x16x32_bf16 v[96:99], v[72:75], v[178:181], v[96:99]
	v_mfma_f32_16x16x32_bf16 v[92:95], v[80:83], v[178:181], v[92:95]
	v_mfma_f32_16x16x32_bf16 v[64:67], v[72:75], v[186:189], v[64:67]
	v_mfma_f32_16x16x32_bf16 v[60:63], v[80:83], v[186:189], v[60:63]
	v_mfma_f32_16x16x32_bf16 v[32:35], v[72:75], v[194:197], v[32:35]
	v_mfma_f32_16x16x32_bf16 v[28:31], v[80:83], v[194:197], v[28:31]
	v_mfma_f32_16x16x32_bf16 v[16:19], v[72:75], v[208:211], v[16:19]
	v_mfma_f32_16x16x32_bf16 v[12:15], v[80:83], v[208:211], v[12:15]
	s_setprio 0
	s_setprio 1
	v_mfma_f32_16x16x32_bf16 v[36:39], v[100:103], v[174:177], v[36:39]
	v_mfma_f32_16x16x32_bf16 v[80:83], v[104:107], v[178:181], v[36:39]
	v_mfma_f32_16x16x32_bf16 v[36:39], v[132:135], v[174:177], v[40:43]
	v_mfma_f32_16x16x32_bf16 v[76:79], v[136:139], v[178:181], v[36:39]
	v_mfma_f32_16x16x32_bf16 v[36:39], v[100:103], v[182:185], v[48:51]
	v_mfma_f32_16x16x32_bf16 v[48:51], v[104:107], v[186:189], v[36:39]
	v_mfma_f32_16x16x32_bf16 v[36:39], v[132:135], v[182:185], v[44:47]
	v_mfma_f32_16x16x32_bf16 v[24:27], v[100:103], v[190:193], v[24:27]
	v_mfma_f32_16x16x32_bf16 v[20:23], v[132:135], v[190:193], v[20:23]
	v_mfma_f32_16x16x32_bf16 v[8:11], v[100:103], v[204:207], v[8:11]
	v_mfma_f32_16x16x32_bf16 v[4:7], v[132:135], v[204:207], v[4:7]
	v_mfma_f32_16x16x32_bf16 v[44:47], v[136:139], v[186:189], v[36:39]
	v_mfma_f32_16x16x32_bf16 v[24:27], v[104:107], v[194:197], v[24:27]
	v_mfma_f32_16x16x32_bf16 v[20:23], v[136:139], v[194:197], v[20:23]
	v_mfma_f32_16x16x32_bf16 v[8:11], v[104:107], v[208:211], v[8:11]
	v_mfma_f32_16x16x32_bf16 v[4:7], v[136:139], v[208:211], v[4:7]
	s_setprio 0
	s_add_i32 s64, s64, 2
	s_add_u32 s6, s6, 0x100
	s_addc_u32 s7, s7, 0
	s_add_u32 s62, s62, 0x100
	s_addc_u32 s63, s63, 0
	s_cmp_gt_u32 s64, 5
	s_cbranch_scc1 .Lee_pj
	s_barrier
	s_branch .LBB0_1135
.Lee_pj:
	s_and_b64 vcc, exec, s[16:17]
	s_cbranch_vccz .LBB0_1138
	s_barrier

;     __device__ __forceinline__ void a_ready(const Unit&) const { if (++ncall == 3 && sig != nullptr && threadIdx.x == 0) __hip_atomic_fetch_add(sig, 1u, __ATOMIC_RELAXED, __HIP_MEMORY_SCOPE_AGENT); }
; #define PG8_STAGE(bufoff, gbase, voff) do { _Pragma("unroll") for (int _i = 0; _i < 2; ++_i) \
;         __builtin_amdgcn_global_load_lds((const unsigned*)((const char*)(gbase) + (voff)[_i]), (PG8_LAS unsigned*)(lds + (bufoff) + ldsw + _i * 8192), 16, 0, 0); } while (0)
; #define PG8_LDA(dst, b, h) do { _Pragma("unroll") for (int m = 0; m < 4; ++m) _Pragma("unroll") for (int k = 0; k < 2; ++k) dst[m][k] = *(const PG8_LAS bf16x8*)(lds + PG8_SA(b, h) + aoff + m * 2048 + k * 1024); } while (0)
; #define PG8_LDB(dst, b, h) do { _Pragma("unroll") for (int n = 0; n < 2; ++n) _Pragma("unroll") for (int k = 0; k < 2; ++k) dst[n][k] = *(const PG8_LAS bf16x8*)(lds + PG8_SB(b, h) + boff + n * 2048 + k * 1024); } while (0)
; #define PG8_WAIT_V(n) asm volatile("s_waitcnt vmcnt(" #n ")" ::: "memory")
; #define PG8_WAIT_L(n) asm volatile("s_waitcnt lgkmcnt(" #n ")" ::: "memory")
; #define PG8_BAR __builtin_amdgcn_s_barrier()
; template <class Epi, class Sched, bool ALIGN_EPI = false, bool SP2 = false>
; __device__ __forceinline__ void gemm_phase(PG8_LAS unsigned char* lds, const Gemm g, const Sched& S, const Epi& E) {
;     ...
;         for (int t = 0; t < nt; t += 2) {
;             const bool last = (t == nt - 2);
;             const char* a1 = cA + (size_t)(t + 1) * kstep;
;             const char* a2 = last ? nA : cA + (size_t)(t + 2) * kstep; const char* b2 = last ? nB : cB + (size_t)(t + 2) * kstep;
;             const char* a3 = a2 + kstep; const char* b3 = b2 + kstep;
;             if (last && has_next) S.a_ready(nxt);
;             if constexpr (SP2) {
;             PG8_LDB(B0, 0, 0); PG8_LDB(B1, 0, 1); PG8_SCHED; PG8_LDA(At, 0, 0); PG8_STAGE(PG8_SA(1, 1), a1 + hstep, voffA);
;     ...
;             if (PROBE_KIND == 18 && t == 0 && ui > 0 && g.probe) { const unsigned long long tq_ = __builtin_amdgcn_s_memrealtime(); PG8_WAIT_V(8); pg8_probe_acc += (unsigned)(__builtin_amdgcn_s_memrealtime() - tq_); }
;     ...
;             PG8_WAIT_V(8); PG8_WAIT_L(0); PG8_BAR; PG8_MMA(0, 0, At, B0); PG8_MMA(0, 1, At, B1); PG8_BAR; PG8_SCHED;
;             PG8_LDA(At, 0, 1); PG8_STAGE(PG8_SB(0, 0), b2, voffB); PG8_STAGE(PG8_SB(0, 1), b2 + hstep, voffB); PG8_STAGE(PG8_SA(0, 0), a2, voffA);
.LBB0_1477:
	s_add_u32 s0, s26, 0xfffc0080
	s_addc_u32 s1, s27, -1
	s_add_i32 s67, 0, 0x10000
	s_cmp_eq_u32 s66, 12
	s_cselect_b32 s29, s17, s1
	s_cselect_b32 s28, s62, s0
	v_add_u32_e32 v151, s67, v147
	s_cselect_b32 s1, s19, s65
	s_cselect_b32 s0, s63, s64
	s_add_i32 s70, 0, 0x14000
	ds_read_b128 v[142:145], v151
	ds_read_b128 v[152:155], v151 offset:1024
	ds_read_b128 v[156:159], v151 offset:2048
	ds_read_b128 v[160:163], v151 offset:3072
	v_add_u32_e32 v151, s70, v147
	ds_read_b128 v[164:167], v151
	ds_read_b128 v[168:171], v151 offset:1024
	ds_read_b128 v[172:175], v151 offset:2048
	ds_read_b128 v[176:179], v151 offset:3072
	v_lshl_add_u64 v[212:213], s[26:27], 0, v[138:139]
	s_add_i32 m0, s15, 0xc000
	ds_read_b128 v[180:183], v150
	ds_read_b128 v[184:187], v150 offset:1024
	ds_read_b128 v[188:191], v150 offset:2048
	ds_read_b128 v[192:195], v150 offset:3072
	ds_read_b128 v[196:199], v150 offset:4096
	ds_read_b128 v[200:203], v150 offset:5120
	ds_read_b128 v[204:207], v150 offset:6144
	ds_read_b128 v[208:211], v150 offset:7168
	global_load_lds_dwordx4 v[212:213], off
	v_lshl_add_u64 v[212:213], s[26:27], 0, v[140:141]
	s_add_i32 m0, s15, 0xe000
	s_nop 0
	global_load_lds_dwordx4 v[212:213], off
	s_waitcnt vmcnt(8)
	s_waitcnt lgkmcnt(0)
	s_barrier
	s_setprio 1
	s_waitcnt lgkmcnt(0)
	v_mfma_f32_16x16x32_bf16 v[128:131], v[142:145], v[180:183], v[128:131]
	v_mfma_f32_16x16x32_bf16 v[124:127], v[156:159], v[180:183], v[124:127]
	v_mfma_f32_16x16x32_bf16 v[112:115], v[142:145], v[188:191], v[112:115]
	v_mfma_f32_16x16x32_bf16 v[108:111], v[156:159], v[188:191], v[108:111]
	v_mfma_f32_16x16x32_bf16 v[96:99], v[142:145], v[196:199], v[96:99]
	v_mfma_f32_16x16x32_bf16 v[92:95], v[156:159], v[196:199], v[92:95]
	v_mfma_f32_16x16x32_bf16 v[80:83], v[142:145], v[204:207], v[80:83]
	v_mfma_f32_16x16x32_bf16 v[76:79], v[156:159], v[204:207], v[76:79]
	v_mfma_f32_16x16x32_bf16 v[128:131], v[152:155], v[184:187], v[128:131]
	v_mfma_f32_16x16x32_bf16 v[124:127], v[160:163], v[184:187], v[124:127]
	v_mfma_f32_16x16x32_bf16 v[112:115], v[152:155], v[192:195], v[112:115]
	v_mfma_f32_16x16x32_bf16 v[108:111], v[160:163], v[192:195], v[108:111]
	v_mfma_f32_16x16x32_bf16 v[96:99], v[152:155], v[200:203], v[96:99]
	v_mfma_f32_16x16x32_bf16 v[92:95], v[160:163], v[200:203], v[92:95]
	v_mfma_f32_16x16x32_bf16 v[80:83], v[152:155], v[208:211], v[80:83]
	v_mfma_f32_16x16x32_bf16 v[76:79], v[160:163], v[208:211], v[76:79]
	s_setprio 0
	s_setprio 1
	v_mfma_f32_16x16x32_bf16 v[120:123], v[164:167], v[180:183], v[120:123]
	v_mfma_f32_16x16x32_bf16 v[116:119], v[172:175], v[180:183], v[116:119]
	v_mfma_f32_16x16x32_bf16 v[104:107], v[164:167], v[188:191], v[104:107]
	v_mfma_f32_16x16x32_bf16 v[100:103], v[172:175], v[188:191], v[100:103]
	v_mfma_f32_16x16x32_bf16 v[88:91], v[164:167], v[196:199], v[88:91]
	v_mfma_f32_16x16x32_bf16 v[84:87], v[172:175], v[196:199], v[84:87]
	v_mfma_f32_16x16x32_bf16 v[72:75], v[164:167], v[204:207], v[72:75]
	v_mfma_f32_16x16x32_bf16 v[68:71], v[172:175], v[204:207], v[68:71]
	v_mfma_f32_16x16x32_bf16 v[120:123], v[168:171], v[184:187], v[120:123]
	v_mfma_f32_16x16x32_bf16 v[116:119], v[176:179], v[184:187], v[116:119]
	v_mfma_f32_16x16x32_bf16 v[104:107], v[168:171], v[192:195], v[104:107]
	v_mfma_f32_16x16x32_bf16 v[100:103], v[176:179], v[192:195], v[100:103]
	v_mfma_f32_16x16x32_bf16 v[88:91], v[168:171], v[200:203], v[88:91]
	v_mfma_f32_16x16x32_bf16 v[84:87], v[176:179], v[200:203], v[84:87]
	v_mfma_f32_16x16x32_bf16 v[72:75], v[168:171], v[208:211], v[72:75]
	v_mfma_f32_16x16x32_bf16 v[68:71], v[176:179], v[208:211], v[68:71]
	s_setprio 0
	s_barrier
	s_add_i32 s67, s67, s25
	v_lshl_add_u64 v[212:213], s[0:1], 0, v[2:3]
	s_mov_b32 m0, s67
	ds_read_b128 v[180:183], v150 offset:16384
	ds_read_b128 v[184:187], v150 offset:17408
	ds_read_b128 v[188:191], v150 offset:18432
	ds_read_b128 v[192:195], v150 offset:19456
	ds_read_b128 v[196:199], v150 offset:20480
	ds_read_b128 v[200:203], v150 offset:21504
	ds_read_b128 v[204:207], v150 offset:22528
	ds_read_b128 v[208:211], v150 offset:23552
	global_load_lds_dwordx4 v[212:213], off
	s_add_i32 m0, s67, 0x2000
	s_add_u32 s68, s0, 0x40000
	v_lshl_add_u64 v[214:215], s[0:1], 0, v[136:137]
	s_addc_u32 s69, s1, 0
	s_add_i32 s67, s70, s25
	global_load_lds_dwordx4 v[214:215], off
	v_lshl_add_u64 v[216:217], s[68:69], 0, v[2:3]
	s_mov_b32 m0, s67
	v_lshl_add_u64 v[218:219], s[28:29], 0, v[134:135]
	global_load_lds_dwordx4 v[216:217], off
	v_lshl_add_u64 v[216:217], s[68:69], 0, v[136:137]
	s_add_i32 m0, s67, 0x2000
	s_nop 0
	global_load_lds_dwordx4 v[216:217], off
	v_lshl_add_u64 v[216:217], s[28:29], 0, v[132:133]
	s_mov_b32 m0, s15
	s_nop 0
	global_load_lds_dwordx4 v[216:217], off
	s_mov_b32 m0, s21
	s_nop 0
	global_load_lds_dwordx4 v[218:219], off
	s_waitcnt vmcnt(8)
	s_waitcnt lgkmcnt(0)
	s_barrier
; #define PG8_STAGE(bufoff, gbase, voff) do { _Pragma("unroll") for (int _i = 0; _i < 2; ++_i) \
;         __builtin_amdgcn_global_load_lds((const unsigned*)((const char*)(gbase) + (voff)[_i]), (PG8_LAS unsigned*)(lds + (bufoff) + ldsw + _i * 8192), 16, 0, 0); } while (0)
; #define PG8_LDA(dst, b, h) do { _Pragma("unroll") for (int m = 0; m < 4; ++m) _Pragma("unroll") for (int k = 0; k < 2; ++k) dst[m][k] = *(const PG8_LAS bf16x8*)(lds + PG8_SA(b, h) + aoff + m * 2048 + k * 1024); } while (0)
; #define PG8_LDB(dst, b, h) do { _Pragma("unroll") for (int n = 0; n < 2; ++n) _Pragma("unroll") for (int k = 0; k < 2; ++k) dst[n][k] = *(const PG8_LAS bf16x8*)(lds + PG8_SB(b, h) + boff + n * 2048 + k * 1024); } while (0)
; #define PG8_MMA(ai, bj, At, Bt) do { __builtin_amdgcn_s_setprio(1); _Pragma("unroll") for (int m = 0; m < 4; ++m) _Pragma("unroll") for (int n = 0; n < 2; ++n) _Pragma("unroll") for (int k = 0; k < 2; ++k) \
;         acc[ai][bj][m][n] = __builtin_amdgcn_mfma_f32_16x16x32_bf16(Bt[n][k], At[m][k], acc[ai][bj][m][n], 0, 0, 0); __builtin_amdgcn_s_setprio(0); } while (0)
; #define PG8_WAIT_V(n) asm volatile("s_waitcnt vmcnt(" #n ")" ::: "memory")
; #define PG8_WAIT_L(n) asm volatile("s_waitcnt lgkmcnt(" #n ")" ::: "memory")
; #define PG8_BAR __builtin_amdgcn_s_barrier()
; #define PG8_SCHED __builtin_amdgcn_sched_barrier(0)
; template <class Epi, class Sched, bool ALIGN_EPI = false, bool SP2 = false>
; __device__ __forceinline__ void gemm_phase(PG8_LAS unsigned char* lds, const Gemm g, const Sched& S, const Epi& E) {
;     ...
;             PG8_WAIT_V(8); PG8_WAIT_L(0); PG8_BAR; if (cur.half == 0) { PG8_MMA(1, 0, At, B0); PG8_MMA(1, 1, At, B1); } PG8_BAR; PG8_SCHED;
;             PG8_LDB(B0, 1, 0); PG8_LDB(B1, 1, 1); PG8_SCHED; PG8_LDA(At, 1, 0); PG8_STAGE(PG8_SA(0, 1), a2 + hstep, voffA);
;             PG8_WAIT_V(8); PG8_WAIT_L(0); PG8_BAR; PG8_MMA(0, 0, At, B0); PG8_MMA(0, 1, At, B1); PG8_BAR; PG8_SCHED;
	s_setprio 1
	s_waitcnt lgkmcnt(0)
	v_mfma_f32_16x16x32_bf16 v[64:67], v[142:145], v[180:183], v[64:67]
	v_mfma_f32_16x16x32_bf16 v[60:63], v[156:159], v[180:183], v[60:63]
	v_mfma_f32_16x16x32_bf16 v[48:51], v[142:145], v[188:191], v[48:51]
	v_mfma_f32_16x16x32_bf16 v[44:47], v[156:159], v[188:191], v[44:47]
	v_mfma_f32_16x16x32_bf16 v[32:35], v[142:145], v[196:199], v[32:35]
	v_mfma_f32_16x16x32_bf16 v[28:31], v[156:159], v[196:199], v[28:31]
	v_mfma_f32_16x16x32_bf16 v[16:19], v[142:145], v[204:207], v[16:19]
	v_mfma_f32_16x16x32_bf16 v[12:15], v[156:159], v[204:207], v[12:15]
	v_mfma_f32_16x16x32_bf16 v[64:67], v[152:155], v[184:187], v[64:67]
	v_mfma_f32_16x16x32_bf16 v[60:63], v[160:163], v[184:187], v[60:63]
	v_mfma_f32_16x16x32_bf16 v[48:51], v[152:155], v[192:195], v[48:51]
	v_mfma_f32_16x16x32_bf16 v[44:47], v[160:163], v[192:195], v[44:47]
	v_mfma_f32_16x16x32_bf16 v[32:35], v[152:155], v[200:203], v[32:35]
	v_mfma_f32_16x16x32_bf16 v[28:31], v[160:163], v[200:203], v[28:31]
	v_mfma_f32_16x16x32_bf16 v[16:19], v[152:155], v[208:211], v[16:19]
	v_mfma_f32_16x16x32_bf16 v[12:15], v[160:163], v[208:211], v[12:15]
	s_setprio 0
	s_setprio 1
	v_mfma_f32_16x16x32_bf16 v[56:59], v[164:167], v[180:183], v[56:59]
	v_mfma_f32_16x16x32_bf16 v[52:55], v[172:175], v[180:183], v[52:55]
	v_mfma_f32_16x16x32_bf16 v[40:43], v[164:167], v[188:191], v[40:43]
	v_mfma_f32_16x16x32_bf16 v[36:39], v[172:175], v[188:191], v[36:39]
	v_mfma_f32_16x16x32_bf16 v[24:27], v[164:167], v[196:199], v[24:27]
	v_mfma_f32_16x16x32_bf16 v[20:23], v[172:175], v[196:199], v[20:23]
	v_mfma_f32_16x16x32_bf16 v[8:11], v[164:167], v[204:207], v[8:11]
	v_mfma_f32_16x16x32_bf16 v[4:7], v[172:175], v[204:207], v[4:7]
	v_mfma_f32_16x16x32_bf16 v[56:59], v[168:171], v[184:187], v[56:59]
	v_mfma_f32_16x16x32_bf16 v[52:55], v[176:179], v[184:187], v[52:55]
	v_mfma_f32_16x16x32_bf16 v[40:43], v[168:171], v[192:195], v[40:43]
	v_mfma_f32_16x16x32_bf16 v[36:39], v[176:179], v[192:195], v[36:39]
	v_mfma_f32_16x16x32_bf16 v[24:27], v[168:171], v[200:203], v[24:27]
	v_mfma_f32_16x16x32_bf16 v[20:23], v[176:179], v[200:203], v[20:23]
	v_mfma_f32_16x16x32_bf16 v[8:11], v[168:171], v[208:211], v[8:11]
	v_mfma_f32_16x16x32_bf16 v[4:7], v[176:179], v[208:211], v[4:7]
	s_setprio 0
	s_barrier
	s_add_i32 s67, 0, 0x18000
	v_add_u32_e32 v151, s67, v147
	s_add_i32 s68, 0, 0x1c000
	ds_read_b128 v[142:145], v151
	ds_read_b128 v[152:155], v151 offset:1024
	ds_read_b128 v[156:159], v151 offset:2048
	ds_read_b128 v[160:163], v151 offset:3072
	v_add_u32_e32 v151, s68, v147
	ds_read_b128 v[164:167], v151
	ds_read_b128 v[168:171], v151 offset:1024
	ds_read_b128 v[172:175], v151 offset:2048
	ds_read_b128 v[176:179], v151 offset:3072
	s_add_u32 s28, s28, 0x40000
	s_addc_u32 s29, s29, 0
	s_mov_b32 m0, s36
	v_lshl_add_u64 v[220:221], s[28:29], 0, v[132:133]
	ds_read_b128 v[180:183], v150 offset:32768
	ds_read_b128 v[184:187], v150 offset:33792
	ds_read_b128 v[188:191], v150 offset:34816
	ds_read_b128 v[192:195], v150 offset:35840
	ds_read_b128 v[196:199], v150 offset:36864
	ds_read_b128 v[200:203], v150 offset:37888
	ds_read_b128 v[204:207], v150 offset:38912
	ds_read_b128 v[208:211], v150 offset:39936
	global_load_lds_dwordx4 v[220:221], off
	v_lshl_add_u64 v[220:221], s[28:29], 0, v[134:135]
	s_mov_b32 m0, s40
	s_nop 0
	global_load_lds_dwordx4 v[220:221], off
	s_waitcnt vmcnt(8)
	s_waitcnt lgkmcnt(0)
	s_barrier
	s_setprio 1
	s_waitcnt lgkmcnt(0)
	v_mfma_f32_16x16x32_bf16 v[128:131], v[142:145], v[180:183], v[128:131]
	v_mfma_f32_16x16x32_bf16 v[124:127], v[156:159], v[180:183], v[124:127]
	v_mfma_f32_16x16x32_bf16 v[112:115], v[142:145], v[188:191], v[112:115]
	v_mfma_f32_16x16x32_bf16 v[108:111], v[156:159], v[188:191], v[108:111]
	v_mfma_f32_16x16x32_bf16 v[96:99], v[142:145], v[196:199], v[96:99]
	v_mfma_f32_16x16x32_bf16 v[92:95], v[156:159], v[196:199], v[92:95]
	v_mfma_f32_16x16x32_bf16 v[80:83], v[142:145], v[204:207], v[80:83]
	v_mfma_f32_16x16x32_bf16 v[76:79], v[156:159], v[204:207], v[76:79]
	v_mfma_f32_16x16x32_bf16 v[128:131], v[152:155], v[184:187], v[128:131]
	v_mfma_f32_16x16x32_bf16 v[124:127], v[160:163], v[184:187], v[124:127]
	v_mfma_f32_16x16x32_bf16 v[112:115], v[152:155], v[192:195], v[112:115]
	v_mfma_f32_16x16x32_bf16 v[108:111], v[160:163], v[192:195], v[108:111]
	v_mfma_f32_16x16x32_bf16 v[96:99], v[152:155], v[200:203], v[96:99]
	v_mfma_f32_16x16x32_bf16 v[92:95], v[160:163], v[200:203], v[92:95]
	v_mfma_f32_16x16x32_bf16 v[80:83], v[152:155], v[208:211], v[80:83]
	v_mfma_f32_16x16x32_bf16 v[76:79], v[160:163], v[208:211], v[76:79]
	s_setprio 0
	s_setprio 1
	v_mfma_f32_16x16x32_bf16 v[120:123], v[164:167], v[180:183], v[120:123]
	v_mfma_f32_16x16x32_bf16 v[116:119], v[172:175], v[180:183], v[116:119]
	v_mfma_f32_16x16x32_bf16 v[104:107], v[164:167], v[188:191], v[104:107]
	v_mfma_f32_16x16x32_bf16 v[100:103], v[172:175], v[188:191], v[100:103]
	v_mfma_f32_16x16x32_bf16 v[88:91], v[164:167], v[196:199], v[88:91]
	v_mfma_f32_16x16x32_bf16 v[84:87], v[172:175], v[196:199], v[84:87]
	v_mfma_f32_16x16x32_bf16 v[72:75], v[164:167], v[204:207], v[72:75]
	v_mfma_f32_16x16x32_bf16 v[68:71], v[172:175], v[204:207], v[68:71]
	v_mfma_f32_16x16x32_bf16 v[120:123], v[168:171], v[184:187], v[120:123]
	v_mfma_f32_16x16x32_bf16 v[116:119], v[176:179], v[184:187], v[116:119]
	v_mfma_f32_16x16x32_bf16 v[104:107], v[168:171], v[192:195], v[104:107]
	v_mfma_f32_16x16x32_bf16 v[100:103], v[176:179], v[192:195], v[100:103]
	v_mfma_f32_16x16x32_bf16 v[88:91], v[168:171], v[200:203], v[88:91]
	v_mfma_f32_16x16x32_bf16 v[84:87], v[176:179], v[200:203], v[84:87]
	v_mfma_f32_16x16x32_bf16 v[72:75], v[168:171], v[208:211], v[72:75]
	v_mfma_f32_16x16x32_bf16 v[68:71], v[176:179], v[208:211], v[68:71]
	s_setprio 0
	s_barrier
; #define PG8_STAGE(bufoff, gbase, voff) do { _Pragma("unroll") for (int _i = 0; _i < 2; ++_i) \
;         __builtin_amdgcn_global_load_lds((const unsigned*)((const char*)(gbase) + (voff)[_i]), (PG8_LAS unsigned*)(lds + (bufoff) + ldsw + _i * 8192), 16, 0, 0); } while (0)
; #define PG8_LDA(dst, b, h) do { _Pragma("unroll") for (int m = 0; m < 4; ++m) _Pragma("unroll") for (int k = 0; k < 2; ++k) dst[m][k] = *(const PG8_LAS bf16x8*)(lds + PG8_SA(b, h) + aoff + m * 2048 + k * 1024); } while (0)
; #define PG8_MMA(ai, bj, At, Bt) do { __builtin_amdgcn_s_setprio(1); _Pragma("unroll") for (int m = 0; m < 4; ++m) _Pragma("unroll") for (int n = 0; n < 2; ++n) _Pragma("unroll") for (int k = 0; k < 2; ++k) \
;         acc[ai][bj][m][n] = __builtin_amdgcn_mfma_f32_16x16x32_bf16(Bt[n][k], At[m][k], acc[ai][bj][m][n], 0, 0, 0); __builtin_amdgcn_s_setprio(0); } while (0)
; #define PG8_WAIT_V(n) asm volatile("s_waitcnt vmcnt(" #n ")" ::: "memory")
; #define PG8_WAIT_L(n) asm volatile("s_waitcnt lgkmcnt(" #n ")" ::: "memory")
; #define PG8_BAR __builtin_amdgcn_s_barrier()
; #define PG8_SCHED __builtin_amdgcn_sched_barrier(0)
; template <class Epi, class Sched, bool ALIGN_EPI = false, bool SP2 = false>
; __device__ __forceinline__ void gemm_phase(PG8_LAS unsigned char* lds, const Gemm g, const Sched& S, const Epi& E) {
;     ...
;             PG8_LDA(At, 1, 1); PG8_STAGE(PG8_SB(1, 0), b3, voffB); PG8_STAGE(PG8_SB(1, 1), b3 + hstep, voffB); PG8_STAGE(PG8_SA(1, 0), a3, voffA);
;             PG8_WAIT_V(8); PG8_WAIT_L(0); PG8_BAR; if (cur.half == 0) { PG8_MMA(1, 0, At, B0); PG8_MMA(1, 1, At, B1); } PG8_BAR; PG8_SCHED;
;     ...
;         if constexpr (ALIGN_EPI) { if (wr == 0) PG8_BAR; }
	s_add_i32 s28, s67, s25
	v_lshl_add_u64 v[212:213], v[212:213], 0, s[42:43]
	s_mov_b32 m0, s28
	ds_read_b128 v[180:183], v150 offset:49152
	ds_read_b128 v[184:187], v150 offset:50176
	ds_read_b128 v[188:191], v150 offset:51200
	ds_read_b128 v[192:195], v150 offset:52224
	ds_read_b128 v[196:199], v150 offset:53248
	ds_read_b128 v[200:203], v150 offset:54272
	ds_read_b128 v[204:207], v150 offset:55296
	ds_read_b128 v[208:211], v150 offset:56320
	global_load_lds_dwordx4 v[212:213], off
	s_add_i32 m0, s28, 0x2000
	s_add_u32 s0, s0, 0x40080
	v_lshl_add_u64 v[212:213], v[214:215], 0, s[42:43]
	s_addc_u32 s1, s1, 0
	s_add_i32 s28, s68, s25
	global_load_lds_dwordx4 v[212:213], off
	v_lshl_add_u64 v[212:213], s[0:1], 0, v[2:3]
	s_mov_b32 m0, s28
	s_nop 0
	global_load_lds_dwordx4 v[212:213], off
	v_lshl_add_u64 v[212:213], s[0:1], 0, v[136:137]
	s_add_i32 m0, s28, 0x2000
	s_nop 0
	global_load_lds_dwordx4 v[212:213], off
	v_lshl_add_u64 v[212:213], v[216:217], 0, s[42:43]
	s_mov_b32 m0, s41
	s_nop 0
	global_load_lds_dwordx4 v[212:213], off
	v_lshl_add_u64 v[212:213], v[218:219], 0, s[42:43]
	s_mov_b32 m0, s60
	s_nop 0
	global_load_lds_dwordx4 v[212:213], off
	s_waitcnt vmcnt(8)
	s_waitcnt lgkmcnt(0)
	s_barrier
	s_setprio 1
	s_waitcnt lgkmcnt(0)
	v_mfma_f32_16x16x32_bf16 v[64:67], v[142:145], v[180:183], v[64:67]
	v_mfma_f32_16x16x32_bf16 v[60:63], v[156:159], v[180:183], v[60:63]
	v_mfma_f32_16x16x32_bf16 v[48:51], v[142:145], v[188:191], v[48:51]
	v_mfma_f32_16x16x32_bf16 v[44:47], v[156:159], v[188:191], v[44:47]
	v_mfma_f32_16x16x32_bf16 v[32:35], v[142:145], v[196:199], v[32:35]
	v_mfma_f32_16x16x32_bf16 v[28:31], v[156:159], v[196:199], v[28:31]
	v_mfma_f32_16x16x32_bf16 v[16:19], v[142:145], v[204:207], v[16:19]
	v_mfma_f32_16x16x32_bf16 v[12:15], v[156:159], v[204:207], v[12:15]
	v_mfma_f32_16x16x32_bf16 v[64:67], v[152:155], v[184:187], v[64:67]
	v_mfma_f32_16x16x32_bf16 v[60:63], v[160:163], v[184:187], v[60:63]
	v_mfma_f32_16x16x32_bf16 v[48:51], v[152:155], v[192:195], v[48:51]
	v_mfma_f32_16x16x32_bf16 v[44:47], v[160:163], v[192:195], v[44:47]
	v_mfma_f32_16x16x32_bf16 v[32:35], v[152:155], v[200:203], v[32:35]
	v_mfma_f32_16x16x32_bf16 v[28:31], v[160:163], v[200:203], v[28:31]
	v_mfma_f32_16x16x32_bf16 v[16:19], v[152:155], v[208:211], v[16:19]
	v_mfma_f32_16x16x32_bf16 v[12:15], v[160:163], v[208:211], v[12:15]
	s_setprio 0
	s_setprio 1
	v_mfma_f32_16x16x32_bf16 v[56:59], v[164:167], v[180:183], v[56:59]
	v_mfma_f32_16x16x32_bf16 v[52:55], v[172:175], v[180:183], v[52:55]
	v_mfma_f32_16x16x32_bf16 v[40:43], v[164:167], v[188:191], v[40:43]
	v_mfma_f32_16x16x32_bf16 v[36:39], v[172:175], v[188:191], v[36:39]
	v_mfma_f32_16x16x32_bf16 v[24:27], v[164:167], v[196:199], v[24:27]
	v_mfma_f32_16x16x32_bf16 v[20:23], v[172:175], v[196:199], v[20:23]
	v_mfma_f32_16x16x32_bf16 v[8:11], v[164:167], v[204:207], v[8:11]
	v_mfma_f32_16x16x32_bf16 v[4:7], v[172:175], v[204:207], v[4:7]
	v_mfma_f32_16x16x32_bf16 v[56:59], v[168:171], v[184:187], v[56:59]
	v_mfma_f32_16x16x32_bf16 v[52:55], v[176:179], v[184:187], v[52:55]
	v_mfma_f32_16x16x32_bf16 v[40:43], v[168:171], v[192:195], v[40:43]
	v_mfma_f32_16x16x32_bf16 v[36:39], v[176:179], v[192:195], v[36:39]
	v_mfma_f32_16x16x32_bf16 v[24:27], v[168:171], v[200:203], v[24:27]
	v_mfma_f32_16x16x32_bf16 v[20:23], v[176:179], v[200:203], v[20:23]
	v_mfma_f32_16x16x32_bf16 v[8:11], v[168:171], v[208:211], v[8:11]
	v_mfma_f32_16x16x32_bf16 v[4:7], v[176:179], v[208:211], v[4:7]
	s_setprio 0
	s_add_i32 s66, s66, 2
	s_add_u32 s26, s26, 0x100
	s_addc_u32 s27, s27, 0
	s_add_u32 s64, s64, 0x100
	s_addc_u32 s65, s65, 0
	s_cmp_gt_u32 s66, 13
	s_cbranch_scc1 .Lee_gu
	s_barrier
	s_branch .LBB0_1477
.Lee_gu:
	s_and_b64 vcc, exec, s[12:13]
	s_cbranch_vccz .LBB0_1480
	s_barrier
